# v99 + nt on the gn_gate phase's y loads (read once; keeps its output, the out-projection's A operand, in the memory-side cache)
# speedup vs baseline: 1.0047x; 1.0047x over previous
.LBB0_341:
	s_ashr_i32 s10, s4, 3
	s_ashr_i32 s11, s10, 31
	s_lshl_b64 s[10:11], s[10:11], 12
	s_and_b32 s12, s6, 0xe00
	s_or_b32 s10, s10, s12
	v_lshl_add_u64 v[0:1], s[10:11], 0, v[20:21]
	v_readlane_b32 s14, v250, 48
	v_lshlrev_b64 v[4:5], 1, v[0:1]
	v_readlane_b32 s15, v250, 49
	v_lshl_add_u64 v[32:33], s[2:3], 0, v[4:5]
	global_load_dwordx4 v[42:45], v[32:33], off nt
	v_lshl_add_u64 v[0:1], s[14:15], 0, v[4:5]
	global_load_dwordx4 v[0:3], v[0:1], off nt
	s_add_i32 s9, s60, s4
	s_cmp_gt_i32 s9, 0x20fff
	s_cselect_b32 s11, s4, s9
	s_ashr_i32 s10, s11, 3
	s_lshl_b32 s13, s11, 9
	s_ashr_i32 s11, s10, 31
	s_and_b32 s13, s13, 0xe00
	s_lshl_b64 s[10:11], s[10:11], 12
	s_add_i32 s9, s60, s9
	s_or_b32 s10, s10, s13
	s_cmp_gt_i32 s9, 0x20fff
	v_lshl_add_u64 v[4:5], s[10:11], 0, v[20:21]
	s_cselect_b32 s11, s4, s9
	s_ashr_i32 s10, s11, 3
	s_lshl_b32 s13, s11, 9
	s_ashr_i32 s11, s10, 31
	s_and_b32 s13, s13, 0xe00
	s_lshl_b64 s[10:11], s[10:11], 12
	v_lshlrev_b64 v[4:5], 1, v[4:5]
	s_or_b32 s10, s10, s13
	v_lshl_add_u64 v[6:7], s[14:15], 0, v[4:5]
	v_lshl_add_u64 v[30:31], s[2:3], 0, v[4:5]
	v_lshl_add_u64 v[4:5], s[10:11], 0, v[20:21]
	v_lshlrev_b64 v[4:5], 1, v[4:5]
	v_lshl_add_u64 v[8:9], s[14:15], 0, v[4:5]
	v_lshl_add_u64 v[28:29], s[2:3], 0, v[4:5]
	global_load_dwordx4 v[46:49], v[6:7], off nt
	global_load_dwordx4 v[12:15], v[8:9], off nt
	global_load_dwordx4 v[16:19], v[30:31], off nt
	s_nop 0
	global_load_dwordx4 v[8:11], v[28:29], off nt
	s_add_i32 s9, s60, s9
	s_cmp_gt_i32 s9, 0x20fff
	s_cselect_b32 s11, s4, s9
	s_lshl_b32 s4, s12, 2
	v_lshl_add_u64 v[26:27], v[22:23], 0, s[4:5]
	global_load_dwordx4 v[50:53], v[26:27], off offset:16 nt
	global_load_dwordx4 v[54:57], v[26:27], off nt
	s_ashr_i32 s10, s11, 3
	s_lshl_b32 s12, s11, 9
	s_ashr_i32 s11, s10, 31
	s_and_b32 s4, s12, 0xe00
	s_lshl_b64 s[10:11], s[10:11], 12
	s_or_b32 s10, s10, s4
	v_lshl_add_u64 v[4:5], s[10:11], 0, v[20:21]
	s_add_i32 s4, s8, s9
	s_cmp_gt_i32 s4, 0x20fff
	s_waitcnt vmcnt(0)
	v_lshlrev_b32_e32 v62, 16, v43
	v_mul_f32_e32 v73, 0xbfb8aa3b, v62
	v_lshlrev_b32_e32 v41, 16, v0
	v_and_b32_e32 v63, 0xffff0000, v0
	v_add_f32_e32 v0, 0, v41
	v_lshlrev_b32_e32 v65, 16, v1
	v_add_f32_e32 v0, v0, v63
	v_and_b32_e32 v67, 0xffff0000, v1
	v_add_f32_e32 v0, v0, v65
	v_lshlrev_b32_e32 v69, 16, v2
	v_add_f32_e32 v0, v0, v67
	v_and_b32_e32 v71, 0xffff0000, v2
	v_add_f32_e32 v0, v0, v69
	v_lshlrev_b32_e32 v59, 16, v3
	v_add_f32_e32 v0, v0, v71
	v_and_b32_e32 v58, 0xffff0000, v3
	v_add_f32_e32 v0, v0, v59
	v_add_f32_e32 v60, v0, v58
	ds_bpermute_b32 v61, v34, v60
	v_exp_f32_e32 v80, v73
	v_lshlrev_b32_e32 v68, 16, v45
	v_lshlrev_b32_e32 v66, 16, v44
	v_and_b32_e32 v44, 0xffff0000, v44
	s_waitcnt lgkmcnt(0)
	v_add_f32_e32 v61, v60, v61
	ds_bpermute_b32 v64, v35, v61
	v_lshlrev_b32_e32 v60, 16, v42
	v_and_b32_e32 v42, 0xffff0000, v42
	v_mul_f32_e32 v72, 0xbfb8aa3b, v42
	v_exp_f32_e32 v79, v72
	s_waitcnt lgkmcnt(0)
	v_add_f32_e32 v61, v61, v64
	ds_bpermute_b32 v70, v36, v61
	v_and_b32_e32 v64, 0xffff0000, v43
	v_lshlrev_b32_e32 v83, 16, v47
	v_and_b32_e32 v84, 0xffff0000, v47
	v_lshlrev_b32_e32 v81, 16, v46
	s_waitcnt lgkmcnt(0)
	v_add_f32_e32 v43, v61, v70
	ds_bpermute_b32 v61, v37, v43
	v_and_b32_e32 v70, 0xffff0000, v45
	v_mul_f32_e32 v45, 0xbfb8aa3b, v60
	v_exp_f32_e32 v45, v45
	v_and_b32_e32 v82, 0xffff0000, v46
	s_waitcnt lgkmcnt(0)
	v_add_f32_e32 v43, v43, v61
	ds_bpermute_b32 v61, v38, v43
	v_add_f32_e32 v45, 1.0, v45
	v_rcp_f32_e32 v46, v45
	v_mul_f32_e32 v74, 0xbfb8aa3b, v64
	v_mul_f32_e32 v75, 0xbfb8aa3b, v66
	s_waitcnt lgkmcnt(0)
	v_add_f32_e32 v43, v43, v61
	ds_bpermute_b32 v61, v39, v43
	v_mul_f32_e32 v76, 0xbfb8aa3b, v44
	v_mul_f32_e32 v77, 0xbfb8aa3b, v68
	v_mul_f32_e32 v78, 0xbfb8aa3b, v70
	v_exp_f32_e32 v78, v78
	s_waitcnt lgkmcnt(0)
	v_add_f32_e32 v43, v43, v61
	v_fmac_f32_e32 v63, 0xbb000000, v43
	v_mul_f32_e32 v72, 0x3b000000, v43
	v_fmac_f32_e32 v41, 0xbb000000, v43
	v_fmac_f32_e32 v65, 0xbb000000, v43
	v_fmac_f32_e32 v67, 0xbb000000, v43
	v_fmac_f32_e32 v69, 0xbb000000, v43
	v_fmac_f32_e32 v71, 0xbb000000, v43
	v_mul_f32_e32 v43, v63, v63
	v_fmac_f32_e32 v43, v41, v41
	v_fmac_f32_e32 v43, v65, v65
	v_fmac_f32_e32 v43, v67, v67
	v_pk_add_f32 v[58:59], v[58:59], v[72:73] op_sel_hi:[1,0] neg_lo:[0,1] neg_hi:[0,1]
	v_fmac_f32_e32 v43, v69, v69
	v_pk_mul_f32 v[72:73], v[58:59], v[58:59]
	v_fmac_f32_e32 v43, v71, v71
	v_add_f32_e32 v43, v73, v43
	v_add_f32_e32 v43, v72, v43
	ds_bpermute_b32 v61, v34, v43
	v_exp_f32_e32 v72, v74
	v_exp_f32_e32 v73, v75
	v_exp_f32_e32 v74, v76
	v_exp_f32_e32 v75, v77
	s_waitcnt lgkmcnt(0)
	v_add_f32_e32 v43, v43, v61
	ds_bpermute_b32 v61, v35, v43
	v_add_f32_e32 v77, 1.0, v79
	v_add_f32_e32 v79, 1.0, v72
	v_add_f32_e32 v73, 1.0, v73
	v_add_f32_e32 v76, 1.0, v80
	s_waitcnt lgkmcnt(0)
	v_add_f32_e32 v43, v43, v61
	ds_bpermute_b32 v61, v36, v43
	v_add_f32_e32 v80, 1.0, v74
	v_rcp_f32_e32 v74, v73
	v_mov_b32_e32 v73, v56
	v_rcp_f32_e32 v56, v79
	s_waitcnt lgkmcnt(0)
	v_add_f32_e32 v43, v43, v61
	ds_bpermute_b32 v61, v37, v43
	v_rcp_f32_e32 v72, v76
	v_add_f32_e32 v75, 1.0, v75
	v_rcp_f32_e32 v76, v75
	v_mov_b32_e32 v75, v50
	s_waitcnt lgkmcnt(0)
	v_add_f32_e32 v43, v43, v61
	ds_bpermute_b32 v47, v38, v43
	v_rcp_f32_e32 v50, v80
	v_lshlrev_b64 v[0:1], 1, v[4:5]
	v_lshl_add_u64 v[2:3], s[14:15], 0, v[0:1]
	v_lshl_add_u64 v[24:25], s[2:3], 0, v[0:1]
	s_waitcnt lgkmcnt(0)
	v_add_f32_e32 v43, v43, v47
	ds_bpermute_b32 v45, v39, v43
	v_mov_b32_e32 v47, v54
	v_rcp_f32_e32 v54, v77
	v_mov_b32_e32 v77, v52
	global_load_dwordx4 v[4:7], v[2:3], off nt
	s_waitcnt lgkmcnt(0)
	v_add_f32_e32 v43, v43, v45
	v_fmamk_f32 v43, v43, 0x3b000000, v40
	v_rsq_f32_e32 v79, v43
	global_load_dwordx4 v[0:3], v[24:25], off nt
	v_mul_f32_e32 v61, v41, v79
	v_mul_f32_e32 v43, v63, v79
	v_pk_mul_f32 v[46:47], v[46:47], v[60:61]
	v_pk_mul_f32 v[42:43], v[54:55], v[42:43]
	v_mul_f32_e32 v41, v46, v47
	v_mul_f32_e32 v46, v42, v43
	v_add_f32_e32 v42, 0, v81
	v_mul_f32_e32 v63, v65, v79
	v_mul_f32_e32 v65, v67, v79
	v_add_f32_e32 v42, v42, v82
	v_pk_mul_f32 v[54:55], v[72:73], v[62:63]
	v_pk_mul_f32 v[56:57], v[56:57], v[64:65]
	v_add_f32_e32 v42, v42, v83
	v_mul_f32_e32 v47, v54, v55
	v_mul_f32_e32 v54, v56, v57
	v_lshlrev_b32_e32 v56, 16, v48
	v_add_f32_e32 v42, v42, v84
	v_mul_f32_e32 v67, v69, v79
	v_and_b32_e32 v57, 0xffff0000, v48
	v_add_f32_e32 v42, v42, v56
	v_mul_f32_e32 v69, v59, v79
	v_pk_mul_f32 v[60:61], v[74:75], v[66:67]
	v_lshlrev_b32_e32 v59, 16, v49
	v_add_f32_e32 v42, v42, v57
	v_mul_f32_e32 v55, v60, v61
	v_and_b32_e32 v60, 0xffff0000, v49
	v_add_f32_e32 v42, v42, v59
	v_add_f32_e32 v42, v42, v60
	ds_bpermute_b32 v43, v34, v42
	v_add_f32_e32 v48, 1.0, v78
	v_rcp_f32_e32 v52, v48
	v_mul_f32_e32 v45, v71, v79
	v_pk_mul_f32 v[44:45], v[50:51], v[44:45]
	v_pk_mul_f32 v[50:51], v[76:77], v[68:69]
	v_mul_f32_e32 v71, v58, v79
	v_mul_f32_e32 v44, v44, v45
	v_mul_f32_e32 v45, v50, v51
	s_waitcnt lgkmcnt(0)
	v_add_f32_e32 v48, v42, v43
	v_pk_mul_f32 v[42:43], v[52:53], v[70:71]
	ds_bpermute_b32 v49, v35, v48
	v_mul_f32_e32 v50, v42, v43
	v_cvt_pk_bf16_f32 v42, v41, v46
	v_cvt_pk_bf16_f32 v43, v47, v54
	v_cvt_pk_bf16_f32 v44, v55, v44
	v_cvt_pk_bf16_f32 v45, v45, v50
	global_store_dwordx4 v[32:33], v[42:45], off
	global_load_dwordx4 v[42:45], v[26:27], off nt
	s_waitcnt lgkmcnt(0)
	v_add_f32_e32 v41, v48, v49
	ds_bpermute_b32 v46, v36, v41
	v_lshlrev_b32_e32 v50, 16, v17
	v_and_b32_e32 v17, 0xffff0000, v17
	v_lshlrev_b32_e32 v51, 16, v18
	v_and_b32_e32 v18, 0xffff0000, v18
	s_waitcnt lgkmcnt(0)
	v_add_f32_e32 v32, v41, v46
	ds_bpermute_b32 v33, v37, v32
	global_load_dwordx4 v[46:49], v[26:27], off offset:16 nt
	v_lshlrev_b32_e32 v41, 16, v16
	v_mul_f32_e32 v53, 0xbfb8aa3b, v41
	v_exp_f32_e32 v53, v53
	s_waitcnt lgkmcnt(0)
	v_add_f32_e32 v32, v32, v33
	ds_bpermute_b32 v33, v38, v32
	v_and_b32_e32 v16, 0xffff0000, v16
	v_lshlrev_b32_e32 v52, 16, v19
	v_and_b32_e32 v19, 0xffff0000, v19
	s_waitcnt lgkmcnt(0)
	v_add_f32_e32 v32, v32, v33
	ds_bpermute_b32 v33, v39, v32
	s_waitcnt lgkmcnt(0)
	v_add_f32_e32 v32, v32, v33
	v_fmac_f32_e32 v82, 0xbb000000, v32
	v_fmac_f32_e32 v81, 0xbb000000, v32
	v_mul_f32_e32 v33, v82, v82
	v_fmac_f32_e32 v33, v81, v81
	v_fmac_f32_e32 v83, 0xbb000000, v32
	v_fmac_f32_e32 v33, v83, v83
	v_fmac_f32_e32 v84, 0xbb000000, v32
	v_fmac_f32_e32 v33, v84, v84
	v_fmac_f32_e32 v56, 0xbb000000, v32
	v_fmac_f32_e32 v33, v56, v56
	v_fmac_f32_e32 v57, 0xbb000000, v32
	v_fmac_f32_e32 v33, v57, v57
	v_fmac_f32_e32 v59, 0xbb000000, v32
	v_fmac_f32_e32 v33, v59, v59
	v_fmac_f32_e32 v60, 0xbb000000, v32
	v_fmac_f32_e32 v33, v60, v60
	ds_bpermute_b32 v32, v34, v33
	s_waitcnt lgkmcnt(0)
	v_add_f32_e32 v32, v33, v32
	ds_bpermute_b32 v33, v35, v32
	s_waitcnt lgkmcnt(0)
	v_add_f32_e32 v32, v32, v33
	ds_bpermute_b32 v33, v36, v32
	s_waitcnt lgkmcnt(0)
	v_add_f32_e32 v32, v32, v33
	ds_bpermute_b32 v33, v37, v32
	s_waitcnt lgkmcnt(0)
	v_add_f32_e32 v32, v32, v33
	ds_bpermute_b32 v33, v38, v32
	s_waitcnt lgkmcnt(0)
	v_add_f32_e32 v32, v32, v33
	ds_bpermute_b32 v33, v39, v32
	s_waitcnt lgkmcnt(0)
	v_add_f32_e32 v32, v32, v33
	v_fmamk_f32 v32, v32, 0x3b000000, v40
	v_add_f32_e32 v33, 1.0, v53
	v_rcp_f32_e32 v33, v33
	v_rsq_f32_e32 v32, v32
	v_mul_f32_e32 v53, 0xbfb8aa3b, v16
	v_exp_f32_e32 v53, v53
	v_mul_f32_e32 v33, v33, v41
	v_mul_f32_e32 v41, v81, v32
	s_waitcnt vmcnt(1)
	v_mul_f32_e32 v41, v42, v41
	v_add_f32_e32 v42, 1.0, v53
	v_rcp_f32_e32 v42, v42
	v_mul_f32_e32 v33, v33, v41
	v_mul_f32_e32 v41, 0xbfb8aa3b, v50
	v_exp_f32_e32 v41, v41
	v_mul_f32_e32 v16, v42, v16
	v_mul_f32_e32 v42, v82, v32
	v_mul_f32_e32 v42, v43, v42
	v_mul_f32_e32 v16, v16, v42
	v_mul_f32_e32 v42, 0xbfb8aa3b, v17
	v_exp_f32_e32 v42, v42
	v_add_f32_e32 v41, 1.0, v41
	v_rcp_f32_e32 v41, v41
	v_mul_f32_e32 v43, v83, v32
	v_add_f32_e32 v42, 1.0, v42
	v_rcp_f32_e32 v42, v42
	v_mul_f32_e32 v41, v41, v50
	v_mul_f32_e32 v43, v44, v43
	v_mul_f32_e32 v41, v41, v43
	v_mul_f32_e32 v43, 0xbfb8aa3b, v51
	v_exp_f32_e32 v43, v43
	v_mul_f32_e32 v17, v42, v17
	v_mul_f32_e32 v42, v84, v32
	v_mul_f32_e32 v42, v45, v42
	v_mul_f32_e32 v17, v17, v42
	v_mul_f32_e32 v42, 0xbfb8aa3b, v18
	v_add_f32_e32 v43, 1.0, v43
	v_exp_f32_e32 v42, v42
	v_rcp_f32_e32 v43, v43
	v_mul_f32_e32 v45, 0xbfb8aa3b, v52
	v_exp_f32_e32 v45, v45
	v_mul_f32_e32 v44, v56, v32
	v_add_f32_e32 v42, 1.0, v42
	v_mul_f32_e32 v43, v43, v51
	s_waitcnt vmcnt(0)
	v_mul_f32_e32 v44, v46, v44
	v_rcp_f32_e32 v42, v42
	v_mul_f32_e32 v43, v43, v44
	v_add_f32_e32 v44, 1.0, v45
	v_mul_f32_e32 v45, 0xbfb8aa3b, v19
	v_rcp_f32_e32 v44, v44
	v_exp_f32_e32 v45, v45
	v_mul_f32_e32 v18, v42, v18
	v_mul_f32_e32 v42, v57, v32
	v_mul_f32_e32 v42, v47, v42
	v_mul_f32_e32 v18, v18, v42
	v_mul_f32_e32 v42, v44, v52
	v_add_f32_e32 v44, 1.0, v45
	v_rcp_f32_e32 v44, v44
	v_mul_f32_e32 v45, v59, v32
	v_mul_f32_e32 v32, v60, v32
	v_mul_f32_e32 v32, v49, v32
	v_mul_f32_e32 v19, v44, v19
	v_mul_f32_e32 v45, v48, v45
	v_mul_f32_e32 v19, v19, v32
	v_mul_f32_e32 v42, v42, v45
	v_cvt_pk_bf16_f32 v16, v33, v16
	v_cvt_pk_bf16_f32 v17, v41, v17
	v_cvt_pk_bf16_f32 v18, v43, v18
	v_cvt_pk_bf16_f32 v19, v42, v19
	s_cbranch_scc1 .LBB0_343
	global_store_dwordx4 v[30:31], v[16:19], off
.LBB0_343:
	v_lshlrev_b32_e32 v30, 16, v12
	v_and_b32_e32 v31, 0xffff0000, v12
	v_add_f32_e32 v12, 0, v30
	v_lshlrev_b32_e32 v32, 16, v13
	v_add_f32_e32 v12, v12, v31
	v_and_b32_e32 v33, 0xffff0000, v13
	v_add_f32_e32 v12, v12, v32
	v_lshlrev_b32_e32 v41, 16, v14
	v_add_f32_e32 v12, v12, v33
	v_and_b32_e32 v42, 0xffff0000, v14
	v_add_f32_e32 v12, v12, v41
	v_lshlrev_b32_e32 v43, 16, v15
	v_add_f32_e32 v12, v12, v42
	v_and_b32_e32 v44, 0xffff0000, v15
	v_add_f32_e32 v12, v12, v43
	v_add_f32_e32 v12, v12, v44
	ds_bpermute_b32 v13, v34, v12
	v_lshlrev_b32_e32 v47, 16, v8
	v_and_b32_e32 v8, 0xffff0000, v8
	v_lshlrev_b32_e32 v48, 16, v9
	v_mul_f32_e32 v51, 0xbfb8aa3b, v47
	s_waitcnt lgkmcnt(0)
	v_add_f32_e32 v12, v12, v13
	ds_bpermute_b32 v13, v35, v12
	v_mul_f32_e32 v52, 0xbfb8aa3b, v8
	v_mul_f32_e32 v53, 0xbfb8aa3b, v48
	v_and_b32_e32 v9, 0xffff0000, v9
	v_exp_f32_e32 v51, v51
	s_waitcnt lgkmcnt(0)
	v_add_f32_e32 v16, v12, v13
	ds_bpermute_b32 v17, v36, v16
	global_load_dwordx4 v[12:15], v[26:27], off nt
	v_exp_f32_e32 v52, v52
	v_exp_f32_e32 v53, v53
	v_mul_f32_e32 v54, 0xbfb8aa3b, v9
	s_waitcnt lgkmcnt(0)
	v_add_f32_e32 v16, v16, v17
	ds_bpermute_b32 v17, v37, v16
	v_exp_f32_e32 v54, v54
	v_add_f32_e32 v51, 1.0, v51
	v_add_f32_e32 v52, 1.0, v52
	v_add_f32_e32 v53, 1.0, v53
	s_waitcnt lgkmcnt(0)
	v_add_f32_e32 v16, v16, v17
	ds_bpermute_b32 v17, v38, v16
	v_rcp_f32_e32 v51, v51
	v_rcp_f32_e32 v52, v52
	v_rcp_f32_e32 v53, v53
	v_add_f32_e32 v54, 1.0, v54
	s_waitcnt lgkmcnt(0)
	v_add_f32_e32 v45, v16, v17
	global_load_dwordx4 v[16:19], v[26:27], off offset:16 nt
	ds_bpermute_b32 v46, v39, v45
	v_lshlrev_b32_e32 v49, 16, v10
	v_rcp_f32_e32 v54, v54
	v_mul_f32_e32 v55, 0xbfb8aa3b, v49
	v_exp_f32_e32 v55, v55
	s_waitcnt lgkmcnt(0)
	v_add_f32_e32 v45, v45, v46
	v_fmac_f32_e32 v31, 0xbb000000, v45
	v_fmac_f32_e32 v30, 0xbb000000, v45
	v_fmac_f32_e32 v32, 0xbb000000, v45
	v_fmac_f32_e32 v33, 0xbb000000, v45
	v_fmac_f32_e32 v41, 0xbb000000, v45
	v_fmac_f32_e32 v42, 0xbb000000, v45
	v_fmac_f32_e32 v43, 0xbb000000, v45
	v_fmac_f32_e32 v44, 0xbb000000, v45
	v_mul_f32_e32 v45, v31, v31
	v_fmac_f32_e32 v45, v30, v30
	v_fmac_f32_e32 v45, v32, v32
	v_fmac_f32_e32 v45, v33, v33
	v_fmac_f32_e32 v45, v41, v41
	v_fmac_f32_e32 v45, v42, v42
	v_fmac_f32_e32 v45, v43, v43
	v_fmac_f32_e32 v45, v44, v44
	ds_bpermute_b32 v46, v34, v45
	v_mul_f32_e32 v8, v52, v8
	v_and_b32_e32 v10, 0xffff0000, v10
	v_mul_f32_e32 v9, v54, v9
	v_lshlrev_b32_e32 v50, 16, v11
	s_waitcnt lgkmcnt(0)
	v_add_f32_e32 v45, v45, v46
	ds_bpermute_b32 v46, v35, v45
	v_and_b32_e32 v11, 0xffff0000, v11
	s_add_i32 s4, s60, s4
	s_cmp_gt_i32 s4, 0x20fff
	s_waitcnt lgkmcnt(0)
	v_add_f32_e32 v45, v45, v46
	ds_bpermute_b32 v46, v36, v45
	s_waitcnt lgkmcnt(0)
	v_add_f32_e32 v45, v45, v46
	ds_bpermute_b32 v46, v37, v45
	s_waitcnt lgkmcnt(0)
	v_add_f32_e32 v45, v45, v46
	ds_bpermute_b32 v46, v38, v45
	s_waitcnt lgkmcnt(0)
	v_add_f32_e32 v45, v45, v46
	ds_bpermute_b32 v46, v39, v45
	s_waitcnt lgkmcnt(0)
	v_add_f32_e32 v45, v45, v46
	v_fmamk_f32 v45, v45, 0x3b000000, v40
	v_rsq_f32_e32 v45, v45
	v_mul_f32_e32 v46, v51, v47
	v_mul_f32_e32 v47, v53, v48
	v_mul_f32_e32 v31, v31, v45
	v_mul_f32_e32 v32, v32, v45
	s_waitcnt vmcnt(1)
	v_mul_f32_e32 v13, v13, v31
	v_mul_f32_e32 v14, v14, v32
	v_mul_f32_e32 v8, v8, v13
	v_mul_f32_e32 v13, v47, v14
	v_mul_f32_e32 v14, v33, v45
	v_mul_f32_e32 v14, v15, v14
	v_mul_f32_e32 v30, v30, v45
	v_mul_f32_e32 v9, v9, v14
	v_mul_f32_e32 v14, 0xbfb8aa3b, v10
	v_mul_f32_e32 v12, v12, v30
	v_add_f32_e32 v15, 1.0, v55
	v_exp_f32_e32 v14, v14
	v_mul_f32_e32 v30, v41, v45
	v_rcp_f32_e32 v15, v15
	s_waitcnt vmcnt(0)
	v_mul_f32_e32 v16, v16, v30
	v_mul_f32_e32 v30, 0xbfb8aa3b, v50
	v_exp_f32_e32 v30, v30
	v_add_f32_e32 v14, 1.0, v14
	v_mul_f32_e32 v15, v15, v49
	v_rcp_f32_e32 v14, v14
	v_mul_f32_e32 v15, v15, v16
	v_add_f32_e32 v16, 1.0, v30
	v_mul_f32_e32 v30, 0xbfb8aa3b, v11
	v_rcp_f32_e32 v16, v16
	v_exp_f32_e32 v30, v30
	v_mul_f32_e32 v10, v14, v10
	v_mul_f32_e32 v14, v42, v45
	v_mul_f32_e32 v14, v17, v14
	v_mul_f32_e32 v10, v10, v14
	v_mul_f32_e32 v14, v16, v50
	v_add_f32_e32 v16, 1.0, v30
	v_rcp_f32_e32 v16, v16
	v_mul_f32_e32 v17, v43, v45
	v_mul_f32_e32 v17, v18, v17
	v_mul_f32_e32 v12, v46, v12
	v_mul_f32_e32 v11, v16, v11
	v_mul_f32_e32 v16, v44, v45
	v_mul_f32_e32 v16, v19, v16
	v_mul_f32_e32 v11, v11, v16
	v_mul_f32_e32 v14, v14, v17
	v_cvt_pk_bf16_f32 v8, v12, v8
	v_cvt_pk_bf16_f32 v9, v13, v9
	v_cvt_pk_bf16_f32 v10, v15, v10
	v_cvt_pk_bf16_f32 v11, v14, v11
	s_cbranch_scc1 .LBB0_345
	global_store_dwordx4 v[28:29], v[8:11], off
.LBB0_345:
	v_lshlrev_b32_e32 v12, 16, v4
	v_and_b32_e32 v13, 0xffff0000, v4
	v_add_f32_e32 v4, 0, v12
	v_lshlrev_b32_e32 v14, 16, v5
	v_add_f32_e32 v4, v4, v13
	v_and_b32_e32 v15, 0xffff0000, v5
	v_add_f32_e32 v4, v4, v14
	v_lshlrev_b32_e32 v16, 16, v6
	v_add_f32_e32 v4, v4, v15
	v_and_b32_e32 v17, 0xffff0000, v6
	v_add_f32_e32 v4, v4, v16
	v_lshlrev_b32_e32 v18, 16, v7
	v_add_f32_e32 v4, v4, v17
	v_and_b32_e32 v19, 0xffff0000, v7
	v_add_f32_e32 v4, v4, v18
	v_add_f32_e32 v4, v4, v19
	ds_bpermute_b32 v5, v34, v4
	v_lshlrev_b32_e32 v30, 16, v2
	v_mul_f32_e32 v43, 0xbfb8aa3b, v30
	v_exp_f32_e32 v43, v43
	v_and_b32_e32 v2, 0xffff0000, v2
	s_waitcnt lgkmcnt(0)
	v_add_f32_e32 v4, v4, v5
	ds_bpermute_b32 v5, v35, v4
	v_lshlrev_b32_e32 v31, 16, v3
	v_and_b32_e32 v3, 0xffff0000, v3
	s_add_i32 s4, s60, s4
	s_cmp_gt_i32 s4, 0x20fff
	s_waitcnt lgkmcnt(0)
	v_add_f32_e32 v8, v4, v5
	ds_bpermute_b32 v9, v36, v8
	global_load_dwordx4 v[4:7], v[26:27], off nt
	s_waitcnt lgkmcnt(0)
	v_add_f32_e32 v8, v8, v9
	ds_bpermute_b32 v9, v37, v8
	s_waitcnt lgkmcnt(0)
	v_add_f32_e32 v8, v8, v9
	ds_bpermute_b32 v9, v38, v8
	s_waitcnt lgkmcnt(0)
	v_add_f32_e32 v28, v8, v9
	global_load_dwordx4 v[8:11], v[26:27], off offset:16 nt
	ds_bpermute_b32 v29, v39, v28
	v_lshlrev_b32_e32 v26, 16, v0
	v_and_b32_e32 v0, 0xffff0000, v0
	v_mul_f32_e32 v33, 0xbfb8aa3b, v0
	v_exp_f32_e32 v33, v33
	s_waitcnt lgkmcnt(0)
	v_add_f32_e32 v27, v28, v29
	v_fmac_f32_e32 v13, 0xbb000000, v27
	v_fmac_f32_e32 v12, 0xbb000000, v27
	v_fmac_f32_e32 v14, 0xbb000000, v27
	v_fmac_f32_e32 v15, 0xbb000000, v27
	v_fmac_f32_e32 v16, 0xbb000000, v27
	v_fmac_f32_e32 v17, 0xbb000000, v27
	v_fmac_f32_e32 v18, 0xbb000000, v27
	v_fmac_f32_e32 v19, 0xbb000000, v27
	v_mul_f32_e32 v27, v13, v13
	v_fmac_f32_e32 v27, v12, v12
	v_fmac_f32_e32 v27, v14, v14
	v_fmac_f32_e32 v27, v15, v15
	v_fmac_f32_e32 v27, v16, v16
	v_fmac_f32_e32 v27, v17, v17
	v_fmac_f32_e32 v27, v18, v18
	v_fmac_f32_e32 v27, v19, v19
	ds_bpermute_b32 v28, v34, v27
	v_lshlrev_b32_e32 v29, 16, v1
	v_mul_f32_e32 v41, 0xbfb8aa3b, v29
	v_and_b32_e32 v1, 0xffff0000, v1
	v_exp_f32_e32 v41, v41
	s_waitcnt lgkmcnt(0)
	v_add_f32_e32 v27, v27, v28
	ds_bpermute_b32 v28, v35, v27
	v_mul_f32_e32 v42, 0xbfb8aa3b, v1
	v_exp_f32_e32 v42, v42
	v_add_f32_e32 v33, 1.0, v33
	v_add_f32_e32 v41, 1.0, v41
	s_waitcnt lgkmcnt(0)
	v_add_f32_e32 v27, v27, v28
	ds_bpermute_b32 v28, v36, v27
	v_rcp_f32_e32 v33, v33
	v_rcp_f32_e32 v41, v41
	v_add_f32_e32 v42, 1.0, v42
	v_rcp_f32_e32 v42, v42
	s_waitcnt lgkmcnt(0)
	v_add_f32_e32 v27, v27, v28
	ds_bpermute_b32 v28, v37, v27
	v_mul_f32_e32 v0, v33, v0
	v_mul_f32_e32 v1, v42, v1
	v_mul_f32_e32 v32, 0xbfb8aa3b, v26
	v_exp_f32_e32 v32, v32
	s_waitcnt lgkmcnt(0)
	v_add_f32_e32 v27, v27, v28
	ds_bpermute_b32 v28, v38, v27
	v_add_f32_e32 v32, 1.0, v32
	v_rcp_f32_e32 v32, v32
	s_waitcnt lgkmcnt(0)
	v_add_f32_e32 v27, v27, v28
	ds_bpermute_b32 v28, v39, v27
	v_mul_f32_e32 v26, v32, v26
	s_waitcnt lgkmcnt(0)
	v_add_f32_e32 v27, v27, v28
	v_fmamk_f32 v27, v27, 0x3b000000, v40
	v_rsq_f32_e32 v27, v27
	v_mul_f32_e32 v28, v41, v29
	v_mul_f32_e32 v13, v13, v27
	v_mul_f32_e32 v14, v14, v27
	s_waitcnt vmcnt(1)
	v_mul_f32_e32 v5, v5, v13
	v_mul_f32_e32 v6, v6, v14
	v_mul_f32_e32 v0, v0, v5
	v_mul_f32_e32 v5, v28, v6
	v_mul_f32_e32 v6, v15, v27
	v_mul_f32_e32 v6, v7, v6
	v_mul_f32_e32 v12, v12, v27
	v_mul_f32_e32 v1, v1, v6
	v_mul_f32_e32 v6, 0xbfb8aa3b, v2
	v_mul_f32_e32 v4, v4, v12
	v_add_f32_e32 v7, 1.0, v43
	v_exp_f32_e32 v6, v6
	v_mul_f32_e32 v12, v16, v27
	v_rcp_f32_e32 v7, v7
	s_waitcnt vmcnt(0)
	v_mul_f32_e32 v8, v8, v12
	v_mul_f32_e32 v12, 0xbfb8aa3b, v31
	v_exp_f32_e32 v12, v12
	v_add_f32_e32 v6, 1.0, v6
	v_mul_f32_e32 v7, v7, v30
	v_rcp_f32_e32 v6, v6
	v_mul_f32_e32 v7, v7, v8
	v_add_f32_e32 v8, 1.0, v12
	v_mul_f32_e32 v12, 0xbfb8aa3b, v3
	v_rcp_f32_e32 v8, v8
	v_exp_f32_e32 v12, v12
	v_mul_f32_e32 v2, v6, v2
	v_mul_f32_e32 v6, v17, v27
	v_mul_f32_e32 v6, v9, v6
	v_mul_f32_e32 v2, v2, v6
	v_mul_f32_e32 v6, v8, v31
	v_add_f32_e32 v8, 1.0, v12
	v_rcp_f32_e32 v8, v8
	v_mul_f32_e32 v9, v18, v27
	v_mul_f32_e32 v9, v10, v9
	v_mul_f32_e32 v4, v26, v4
	v_mul_f32_e32 v3, v8, v3
	v_mul_f32_e32 v8, v19, v27
	v_mul_f32_e32 v8, v11, v8
	v_mul_f32_e32 v3, v3, v8
	v_mul_f32_e32 v6, v6, v9
	v_cvt_pk_bf16_f32 v0, v4, v0
	v_cvt_pk_bf16_f32 v1, v5, v1
	v_cvt_pk_bf16_f32 v2, v7, v2
	v_cvt_pk_bf16_f32 v3, v6, v3
	s_cbranch_scc1 .LBB0_340
	global_store_dwordx4 v[24:25], v[0:3], off
	s_branch .LBB0_340
